# instruction selection: MoE epilogue store addresses as one 64-bit add per row group (up and down), plus v_mov_b64 accumulator init
# baseline (speedup 1.0000x reference)
; __device__ __forceinline__ unsigned cvt_pk_bf16(float lo, float hi) { unsigned r; asm volatile("v_cvt_pk_bf16_f32 %0, %1, %2" : "=v"(r) : "v"(lo), "v"(hi)); return r; }
;     __device__ __forceinline__ void operator()(const pg8::f32x4 (&acc)[2][2][4][2], const pg8::Unit& u, int wr, int wc, int fr, int fq) const {
;     ...
;         const int colj = u.pn * 128 + wc * 32 + 8 * fq;
;         const float* bg = b_up + u.e * 2048 + colj;
;         f32x4 bgv[2], blv[2];
; #pragma unroll
;         for (int n = 0; n < 2; ++n) { bgv[n] = *(const f32x4*)(bg + 4 * n); blv[n] = *(const f32x4*)(bg + 1024 + 4 * n); }
; #pragma unroll
;         for (int ai = 0; ai < 2; ++ai)
; #pragma unroll
;             for (int m = 0; m < 4; ++m) {
;                 const int row = u.pm + ai * 128 + wr * 64 + m * 16 + fr;
;                 float a[8];
; #pragma unroll
;                 for (int n = 0; n < 2; ++n)
; #pragma unroll
;                     for (int j = 0; j < 4; ++j) {
;                         const float g = fminf(acc[ai][0][m][n][j] + bgv[n][j], 7.f);
;                         const float l = fminf(fmaxf(acc[ai][1][m][n][j] + blv[n][j], -7.f), 7.f);
;                         const float sg = __builtin_amdgcn_rcpf(1.f + __builtin_amdgcn_exp2f(-1.702f * 1.4426950408889634f * g));
;                         a[n * 4 + j] = g * sg * (l + 1.f);
;                     }
;                 pg8::u32x4 w; w.x = pg8::cvt_pk_bf16(a[0], a[1]); w.y = pg8::cvt_pk_bf16(a[2], a[3]); w.z = pg8::cvt_pk_bf16(a[4], a[5]); w.w = pg8::cvt_pk_bf16(a[6], a[7]);
;                 *(pg8::u32x4*)(ACT + (size_t)row * 1024 + colj) = w;
.Lup_epi_nonext:
	s_andn2_b64 vcc, exec, s[44:45]
	s_mov_b32 s4, 0xc0c00000
	s_mov_b64 s[72:73], 0x8000
	s_mov_b64 s[74:75], 0x28000
	v_mov_b32_e32 v198, 0x41000000
	v_min_f32_e32 v132, 0x40e00000, v128
	v_min_f32_e32 v133, 0x40e00000, v129
	v_min_f32_e32 v134, 0x40e00000, v130
	v_min_f32_e32 v135, 0x40e00000, v131
	v_min_f32_e32 v136, 0x40e00000, v124
	v_min_f32_e32 v137, 0x40e00000, v125
	v_min_f32_e32 v138, 0x40e00000, v126
	v_min_f32_e32 v139, 0x40e00000, v127
	v_mul_f32_e32 v140, 0xc01d265f, v132
	v_mul_f32_e32 v141, 0xc01d265f, v133
	v_mul_f32_e32 v142, 0xc01d265f, v134
	v_mul_f32_e32 v143, 0xc01d265f, v135
	v_mul_f32_e32 v144, 0xc01d265f, v136
	v_mul_f32_e32 v145, 0xc01d265f, v137
	v_mul_f32_e32 v146, 0xc01d265f, v138
	v_mul_f32_e32 v147, 0xc01d265f, v139
	v_exp_f32_e32 v140, v140
	v_exp_f32_e32 v141, v141
	v_exp_f32_e32 v142, v142
	v_exp_f32_e32 v143, v143
	v_exp_f32_e32 v144, v144
	v_exp_f32_e32 v145, v145
	v_exp_f32_e32 v146, v146
	v_exp_f32_e32 v147, v147
	v_med3_f32 v182, v96, s4, v198
	v_med3_f32 v183, v97, s4, v198
	v_med3_f32 v184, v98, s4, v198
	v_med3_f32 v185, v99, s4, v198
	v_med3_f32 v186, v92, s4, v198
	v_med3_f32 v187, v93, s4, v198
	v_med3_f32 v188, v94, s4, v198
	v_med3_f32 v189, v95, s4, v198
	v_add_f32_e32 v140, 1.0, v140
	v_add_f32_e32 v141, 1.0, v141
	v_add_f32_e32 v142, 1.0, v142
	v_add_f32_e32 v143, 1.0, v143
	v_add_f32_e32 v144, 1.0, v144
	v_add_f32_e32 v145, 1.0, v145
	v_add_f32_e32 v146, 1.0, v146
	v_add_f32_e32 v147, 1.0, v147
	v_rcp_f32_e32 v140, v140
	v_rcp_f32_e32 v141, v141
	v_rcp_f32_e32 v142, v142
	v_rcp_f32_e32 v143, v143
	v_rcp_f32_e32 v144, v144
	v_rcp_f32_e32 v145, v145
	v_rcp_f32_e32 v146, v146
	v_rcp_f32_e32 v147, v147
	v_mul_f32_e32 v132, v132, v182
	v_mul_f32_e32 v133, v133, v183
	v_mul_f32_e32 v134, v134, v184
	v_mul_f32_e32 v135, v135, v185
	v_mul_f32_e32 v136, v136, v186
	v_mul_f32_e32 v137, v137, v187
	v_mul_f32_e32 v138, v138, v188
	v_mul_f32_e32 v139, v139, v189
	v_add_u32_e32 v196, s48, v169
	v_ashrrev_i32_e32 v197, 31, v196
	v_lshlrev_b64 v[194:195], 11, v[196:197]
	v_lshl_add_u64 v[194:195], s[90:91], 0, v[194:195]
	v_lshl_add_u64 v[194:195], v[194:195], 0, v[160:161]
	v_mul_f32_e32 v132, v132, v140
	v_mul_f32_e32 v133, v133, v141
	v_mul_f32_e32 v134, v134, v142
	v_mul_f32_e32 v135, v135, v143
	v_mul_f32_e32 v136, v136, v144
	v_mul_f32_e32 v137, v137, v145
	v_mul_f32_e32 v138, v138, v146
	v_mul_f32_e32 v139, v139, v147
	v_cvt_pk_bf16_f32 v190, v132, v133
	v_cvt_pk_bf16_f32 v191, v134, v135
	v_cvt_pk_bf16_f32 v192, v136, v137
	v_cvt_pk_bf16_f32 v193, v138, v139
	global_store_dwordx4 v[194:195], v[190:193], off
	v_min_f32_e32 v132, 0x40e00000, v120
	v_min_f32_e32 v133, 0x40e00000, v121
	v_min_f32_e32 v134, 0x40e00000, v122
	v_min_f32_e32 v135, 0x40e00000, v123
	v_min_f32_e32 v136, 0x40e00000, v116
	v_min_f32_e32 v137, 0x40e00000, v117
	v_min_f32_e32 v138, 0x40e00000, v118
	v_min_f32_e32 v139, 0x40e00000, v119
	v_mul_f32_e32 v140, 0xc01d265f, v132
	v_mul_f32_e32 v141, 0xc01d265f, v133
	v_mul_f32_e32 v142, 0xc01d265f, v134
	v_mul_f32_e32 v143, 0xc01d265f, v135
	v_mul_f32_e32 v144, 0xc01d265f, v136
	v_mul_f32_e32 v145, 0xc01d265f, v137
	v_mul_f32_e32 v146, 0xc01d265f, v138
	v_mul_f32_e32 v147, 0xc01d265f, v139
	v_exp_f32_e32 v140, v140
	v_exp_f32_e32 v141, v141
	v_exp_f32_e32 v142, v142
	v_exp_f32_e32 v143, v143
	v_exp_f32_e32 v144, v144
	v_exp_f32_e32 v145, v145
	v_exp_f32_e32 v146, v146
	v_exp_f32_e32 v147, v147
	v_med3_f32 v182, v88, s4, v198
	v_med3_f32 v183, v89, s4, v198
	v_med3_f32 v184, v90, s4, v198
	v_med3_f32 v185, v91, s4, v198
	v_med3_f32 v186, v84, s4, v198
	v_med3_f32 v187, v85, s4, v198
	v_med3_f32 v188, v86, s4, v198
	v_med3_f32 v189, v87, s4, v198
	v_add_f32_e32 v140, 1.0, v140
	v_add_f32_e32 v141, 1.0, v141
	v_add_f32_e32 v142, 1.0, v142
	v_add_f32_e32 v143, 1.0, v143
	v_add_f32_e32 v144, 1.0, v144
	v_add_f32_e32 v145, 1.0, v145
	v_add_f32_e32 v146, 1.0, v146
	v_add_f32_e32 v147, 1.0, v147
	v_rcp_f32_e32 v140, v140
	v_rcp_f32_e32 v141, v141
	v_rcp_f32_e32 v142, v142
	v_rcp_f32_e32 v143, v143
	v_rcp_f32_e32 v144, v144
	v_rcp_f32_e32 v145, v145
	v_rcp_f32_e32 v146, v146
	v_rcp_f32_e32 v147, v147
	v_mul_f32_e32 v132, v132, v182
	v_mul_f32_e32 v133, v133, v183
	v_mul_f32_e32 v134, v134, v184
	v_mul_f32_e32 v135, v135, v185
	v_mul_f32_e32 v136, v136, v186
	v_mul_f32_e32 v137, v137, v187
	v_mul_f32_e32 v138, v138, v188
	v_mul_f32_e32 v139, v139, v189
	v_lshl_add_u64 v[194:195], v[194:195], 0, s[72:73]
	v_mul_f32_e32 v132, v132, v140
	v_mul_f32_e32 v133, v133, v141
	v_mul_f32_e32 v134, v134, v142
	v_mul_f32_e32 v135, v135, v143
	v_mul_f32_e32 v136, v136, v144
	v_mul_f32_e32 v137, v137, v145
	v_mul_f32_e32 v138, v138, v146
	v_mul_f32_e32 v139, v139, v147
	v_cvt_pk_bf16_f32 v190, v132, v133
	v_cvt_pk_bf16_f32 v191, v134, v135
	v_cvt_pk_bf16_f32 v192, v136, v137
	v_cvt_pk_bf16_f32 v193, v138, v139
	global_store_dwordx4 v[194:195], v[190:193], off
	v_min_f32_e32 v132, 0x40e00000, v112
	v_min_f32_e32 v133, 0x40e00000, v113
	v_min_f32_e32 v134, 0x40e00000, v114
	v_min_f32_e32 v135, 0x40e00000, v115
	v_min_f32_e32 v136, 0x40e00000, v108
	v_min_f32_e32 v137, 0x40e00000, v109
	v_min_f32_e32 v138, 0x40e00000, v110
	v_min_f32_e32 v139, 0x40e00000, v111
	v_mul_f32_e32 v140, 0xc01d265f, v132
	v_mul_f32_e32 v141, 0xc01d265f, v133
	v_mul_f32_e32 v142, 0xc01d265f, v134
	v_mul_f32_e32 v143, 0xc01d265f, v135
	v_mul_f32_e32 v144, 0xc01d265f, v136
	v_mul_f32_e32 v145, 0xc01d265f, v137
	v_mul_f32_e32 v146, 0xc01d265f, v138
	v_mul_f32_e32 v147, 0xc01d265f, v139
	v_exp_f32_e32 v140, v140
	v_exp_f32_e32 v141, v141
	v_exp_f32_e32 v142, v142
	v_exp_f32_e32 v143, v143
	v_exp_f32_e32 v144, v144
; __device__ __forceinline__ unsigned cvt_pk_bf16(float lo, float hi) { unsigned r; asm volatile("v_cvt_pk_bf16_f32 %0, %1, %2" : "=v"(r) : "v"(lo), "v"(hi)); return r; }
;     __device__ __forceinline__ void operator()(const pg8::f32x4 (&acc)[2][2][4][2], const pg8::Unit& u, int wr, int wc, int fr, int fq) const {
;     ...
;             for (int m = 0; m < 4; ++m) {
;                 const int row = u.pm + ai * 128 + wr * 64 + m * 16 + fr;
;                 float a[8];
; #pragma unroll
;                 for (int n = 0; n < 2; ++n)
; #pragma unroll
;                     for (int j = 0; j < 4; ++j) {
;                         const float g = fminf(acc[ai][0][m][n][j] + bgv[n][j], 7.f);
;                         const float l = fminf(fmaxf(acc[ai][1][m][n][j] + blv[n][j], -7.f), 7.f);
;                         const float sg = __builtin_amdgcn_rcpf(1.f + __builtin_amdgcn_exp2f(-1.702f * 1.4426950408889634f * g));
;                         a[n * 4 + j] = g * sg * (l + 1.f);
;                     }
;                 pg8::u32x4 w; w.x = pg8::cvt_pk_bf16(a[0], a[1]); w.y = pg8::cvt_pk_bf16(a[2], a[3]); w.z = pg8::cvt_pk_bf16(a[4], a[5]); w.w = pg8::cvt_pk_bf16(a[6], a[7]);
;                 *(pg8::u32x4*)(ACT + (size_t)row * 1024 + colj) = w;
	v_exp_f32_e32 v145, v145
	v_exp_f32_e32 v146, v146
	v_exp_f32_e32 v147, v147
	v_med3_f32 v182, v80, s4, v198
	v_med3_f32 v183, v81, s4, v198
	v_med3_f32 v184, v82, s4, v198
	v_med3_f32 v185, v83, s4, v198
	v_med3_f32 v186, v76, s4, v198
	v_med3_f32 v187, v77, s4, v198
	v_med3_f32 v188, v78, s4, v198
	v_med3_f32 v189, v79, s4, v198
	v_add_f32_e32 v140, 1.0, v140
	v_add_f32_e32 v141, 1.0, v141
	v_add_f32_e32 v142, 1.0, v142
	v_add_f32_e32 v143, 1.0, v143
	v_add_f32_e32 v144, 1.0, v144
	v_add_f32_e32 v145, 1.0, v145
	v_add_f32_e32 v146, 1.0, v146
	v_add_f32_e32 v147, 1.0, v147
	v_rcp_f32_e32 v140, v140
	v_rcp_f32_e32 v141, v141
	v_rcp_f32_e32 v142, v142
	v_rcp_f32_e32 v143, v143
	v_rcp_f32_e32 v144, v144
	v_rcp_f32_e32 v145, v145
	v_rcp_f32_e32 v146, v146
	v_rcp_f32_e32 v147, v147
	v_mul_f32_e32 v132, v132, v182
	v_mul_f32_e32 v133, v133, v183
	v_mul_f32_e32 v134, v134, v184
	v_mul_f32_e32 v135, v135, v185
	v_mul_f32_e32 v136, v136, v186
	v_mul_f32_e32 v137, v137, v187
	v_mul_f32_e32 v138, v138, v188
	v_mul_f32_e32 v139, v139, v189
	v_lshl_add_u64 v[194:195], v[194:195], 0, s[72:73]
	v_mul_f32_e32 v132, v132, v140
	v_mul_f32_e32 v133, v133, v141
	v_mul_f32_e32 v134, v134, v142
	v_mul_f32_e32 v135, v135, v143
	v_mul_f32_e32 v136, v136, v144
	v_mul_f32_e32 v137, v137, v145
	v_mul_f32_e32 v138, v138, v146
	v_mul_f32_e32 v139, v139, v147
	v_cvt_pk_bf16_f32 v190, v132, v133
	v_cvt_pk_bf16_f32 v191, v134, v135
	v_cvt_pk_bf16_f32 v192, v136, v137
	v_cvt_pk_bf16_f32 v193, v138, v139
	global_store_dwordx4 v[194:195], v[190:193], off
	v_min_f32_e32 v132, 0x40e00000, v104
	v_min_f32_e32 v133, 0x40e00000, v105
	v_min_f32_e32 v134, 0x40e00000, v106
	v_min_f32_e32 v135, 0x40e00000, v107
	v_min_f32_e32 v136, 0x40e00000, v100
	v_min_f32_e32 v137, 0x40e00000, v101
	v_min_f32_e32 v138, 0x40e00000, v102
	v_min_f32_e32 v139, 0x40e00000, v103
	v_mul_f32_e32 v140, 0xc01d265f, v132
	v_mul_f32_e32 v141, 0xc01d265f, v133
	v_mul_f32_e32 v142, 0xc01d265f, v134
	v_mul_f32_e32 v143, 0xc01d265f, v135
	v_mul_f32_e32 v144, 0xc01d265f, v136
	v_mul_f32_e32 v145, 0xc01d265f, v137
	v_mul_f32_e32 v146, 0xc01d265f, v138
	v_mul_f32_e32 v147, 0xc01d265f, v139
	v_exp_f32_e32 v140, v140
	v_exp_f32_e32 v141, v141
	v_exp_f32_e32 v142, v142
	v_exp_f32_e32 v143, v143
	v_exp_f32_e32 v144, v144
	v_exp_f32_e32 v145, v145
	v_exp_f32_e32 v146, v146
	v_exp_f32_e32 v147, v147
	v_med3_f32 v182, v72, s4, v198
	v_med3_f32 v183, v73, s4, v198
	v_med3_f32 v184, v74, s4, v198
	v_med3_f32 v185, v75, s4, v198
	v_med3_f32 v186, v68, s4, v198
	v_med3_f32 v187, v69, s4, v198
	v_med3_f32 v188, v70, s4, v198
	v_med3_f32 v189, v71, s4, v198
	v_add_f32_e32 v140, 1.0, v140
	v_add_f32_e32 v141, 1.0, v141
	v_add_f32_e32 v142, 1.0, v142
	v_add_f32_e32 v143, 1.0, v143
	v_add_f32_e32 v144, 1.0, v144
	v_add_f32_e32 v145, 1.0, v145
	v_add_f32_e32 v146, 1.0, v146
	v_add_f32_e32 v147, 1.0, v147
	v_rcp_f32_e32 v140, v140
	v_rcp_f32_e32 v141, v141
	v_rcp_f32_e32 v142, v142
	v_rcp_f32_e32 v143, v143
	v_rcp_f32_e32 v144, v144
	v_rcp_f32_e32 v145, v145
	v_rcp_f32_e32 v146, v146
	v_rcp_f32_e32 v147, v147
	v_mul_f32_e32 v132, v132, v182
	v_mul_f32_e32 v133, v133, v183
	v_mul_f32_e32 v134, v134, v184
	v_mul_f32_e32 v135, v135, v185
	v_mul_f32_e32 v136, v136, v186
	v_mul_f32_e32 v137, v137, v187
	v_mul_f32_e32 v138, v138, v188
	v_mul_f32_e32 v139, v139, v189
	v_lshl_add_u64 v[194:195], v[194:195], 0, s[72:73]
	v_mul_f32_e32 v132, v132, v140
	v_mul_f32_e32 v133, v133, v141
	v_mul_f32_e32 v134, v134, v142
	v_mul_f32_e32 v135, v135, v143
	v_mul_f32_e32 v136, v136, v144
	v_mul_f32_e32 v137, v137, v145
	v_mul_f32_e32 v138, v138, v146
	v_mul_f32_e32 v139, v139, v147
	v_cvt_pk_bf16_f32 v190, v132, v133
	v_cvt_pk_bf16_f32 v191, v134, v135
	v_cvt_pk_bf16_f32 v192, v136, v137
	v_cvt_pk_bf16_f32 v193, v138, v139
	global_store_dwordx4 v[194:195], v[190:193], off
	v_min_f32_e32 v132, 0x40e00000, v64
	v_min_f32_e32 v133, 0x40e00000, v65
	v_min_f32_e32 v134, 0x40e00000, v66
	v_min_f32_e32 v135, 0x40e00000, v67
	v_min_f32_e32 v136, 0x40e00000, v60
	v_min_f32_e32 v137, 0x40e00000, v61
	v_min_f32_e32 v138, 0x40e00000, v62
	v_min_f32_e32 v139, 0x40e00000, v63
	v_mul_f32_e32 v140, 0xc01d265f, v132
	v_mul_f32_e32 v141, 0xc01d265f, v133
	v_mul_f32_e32 v142, 0xc01d265f, v134
	v_mul_f32_e32 v143, 0xc01d265f, v135
	v_mul_f32_e32 v144, 0xc01d265f, v136
	v_mul_f32_e32 v145, 0xc01d265f, v137
	v_mul_f32_e32 v146, 0xc01d265f, v138
	v_mul_f32_e32 v147, 0xc01d265f, v139
	v_exp_f32_e32 v140, v140
	v_exp_f32_e32 v141, v141
	v_exp_f32_e32 v142, v142
	v_exp_f32_e32 v143, v143
	v_exp_f32_e32 v144, v144
	v_exp_f32_e32 v145, v145
	v_exp_f32_e32 v146, v146
	v_exp_f32_e32 v147, v147
	v_med3_f32 v182, v32, s4, v198
	v_med3_f32 v183, v33, s4, v198
	v_med3_f32 v184, v34, s4, v198
	v_med3_f32 v185, v35, s4, v198
	v_med3_f32 v186, v28, s4, v198
	v_med3_f32 v187, v29, s4, v198
	v_med3_f32 v188, v30, s4, v198
	v_med3_f32 v189, v31, s4, v198
	v_add_f32_e32 v140, 1.0, v140
	v_add_f32_e32 v141, 1.0, v141
	v_add_f32_e32 v142, 1.0, v142
	v_add_f32_e32 v143, 1.0, v143
	v_add_f32_e32 v144, 1.0, v144
	v_add_f32_e32 v145, 1.0, v145
	v_add_f32_e32 v146, 1.0, v146
	v_add_f32_e32 v147, 1.0, v147
	v_rcp_f32_e32 v140, v140
	v_rcp_f32_e32 v141, v141
	v_rcp_f32_e32 v142, v142
	v_rcp_f32_e32 v143, v143
	v_rcp_f32_e32 v144, v144
	v_rcp_f32_e32 v145, v145
	v_rcp_f32_e32 v146, v146
	v_rcp_f32_e32 v147, v147
	v_mul_f32_e32 v132, v132, v182
	v_mul_f32_e32 v133, v133, v183
	v_mul_f32_e32 v134, v134, v184
	v_mul_f32_e32 v135, v135, v185
	v_mul_f32_e32 v136, v136, v186
	v_mul_f32_e32 v137, v137, v187
	v_mul_f32_e32 v138, v138, v188
	v_mul_f32_e32 v139, v139, v189
	v_lshl_add_u64 v[194:195], v[194:195], 0, s[74:75]
; __device__ __forceinline__ unsigned cvt_pk_bf16(float lo, float hi) { unsigned r; asm volatile("v_cvt_pk_bf16_f32 %0, %1, %2" : "=v"(r) : "v"(lo), "v"(hi)); return r; }
;     __device__ __forceinline__ void operator()(const pg8::f32x4 (&acc)[2][2][4][2], const pg8::Unit& u, int wr, int wc, int fr, int fq) const {
;     ...
;             for (int m = 0; m < 4; ++m) {
;                 const int row = u.pm + ai * 128 + wr * 64 + m * 16 + fr;
;                 float a[8];
; #pragma unroll
;                 for (int n = 0; n < 2; ++n)
; #pragma unroll
;                     for (int j = 0; j < 4; ++j) {
;                         const float g = fminf(acc[ai][0][m][n][j] + bgv[n][j], 7.f);
;                         const float l = fminf(fmaxf(acc[ai][1][m][n][j] + blv[n][j], -7.f), 7.f);
;                         const float sg = __builtin_amdgcn_rcpf(1.f + __builtin_amdgcn_exp2f(-1.702f * 1.4426950408889634f * g));
;                         a[n * 4 + j] = g * sg * (l + 1.f);
;                     }
;                 pg8::u32x4 w; w.x = pg8::cvt_pk_bf16(a[0], a[1]); w.y = pg8::cvt_pk_bf16(a[2], a[3]); w.z = pg8::cvt_pk_bf16(a[4], a[5]); w.w = pg8::cvt_pk_bf16(a[6], a[7]);
;                 *(pg8::u32x4*)(ACT + (size_t)row * 1024 + colj) = w;
	v_mul_f32_e32 v132, v132, v140
	v_mul_f32_e32 v133, v133, v141
	v_mul_f32_e32 v134, v134, v142
	v_mul_f32_e32 v135, v135, v143
	v_mul_f32_e32 v136, v136, v144
	v_mul_f32_e32 v137, v137, v145
	v_mul_f32_e32 v138, v138, v146
	v_mul_f32_e32 v139, v139, v147
	v_cvt_pk_bf16_f32 v190, v132, v133
	v_cvt_pk_bf16_f32 v191, v134, v135
	v_cvt_pk_bf16_f32 v192, v136, v137
	v_cvt_pk_bf16_f32 v193, v138, v139
	global_store_dwordx4 v[194:195], v[190:193], off
	v_min_f32_e32 v132, 0x40e00000, v56
	v_min_f32_e32 v133, 0x40e00000, v57
	v_min_f32_e32 v134, 0x40e00000, v58
	v_min_f32_e32 v135, 0x40e00000, v59
	v_min_f32_e32 v136, 0x40e00000, v52
	v_min_f32_e32 v137, 0x40e00000, v53
	v_min_f32_e32 v138, 0x40e00000, v54
	v_min_f32_e32 v139, 0x40e00000, v55
	v_mul_f32_e32 v140, 0xc01d265f, v132
	v_mul_f32_e32 v141, 0xc01d265f, v133
	v_mul_f32_e32 v142, 0xc01d265f, v134
	v_mul_f32_e32 v143, 0xc01d265f, v135
	v_mul_f32_e32 v144, 0xc01d265f, v136
	v_mul_f32_e32 v145, 0xc01d265f, v137
	v_mul_f32_e32 v146, 0xc01d265f, v138
	v_mul_f32_e32 v147, 0xc01d265f, v139
	v_exp_f32_e32 v140, v140
	v_exp_f32_e32 v141, v141
	v_exp_f32_e32 v142, v142
	v_exp_f32_e32 v143, v143
	v_exp_f32_e32 v144, v144
	v_exp_f32_e32 v145, v145
	v_exp_f32_e32 v146, v146
	v_exp_f32_e32 v147, v147
	v_med3_f32 v182, v24, s4, v198
	v_med3_f32 v183, v25, s4, v198
	v_med3_f32 v184, v26, s4, v198
	v_med3_f32 v185, v27, s4, v198
	v_med3_f32 v186, v20, s4, v198
	v_med3_f32 v187, v21, s4, v198
	v_med3_f32 v188, v22, s4, v198
	v_med3_f32 v189, v23, s4, v198
	v_add_f32_e32 v140, 1.0, v140
	v_add_f32_e32 v141, 1.0, v141
	v_add_f32_e32 v142, 1.0, v142
	v_add_f32_e32 v143, 1.0, v143
	v_add_f32_e32 v144, 1.0, v144
	v_add_f32_e32 v145, 1.0, v145
	v_add_f32_e32 v146, 1.0, v146
	v_add_f32_e32 v147, 1.0, v147
	v_rcp_f32_e32 v140, v140
	v_rcp_f32_e32 v141, v141
	v_rcp_f32_e32 v142, v142
	v_rcp_f32_e32 v143, v143
	v_rcp_f32_e32 v144, v144
	v_rcp_f32_e32 v145, v145
	v_rcp_f32_e32 v146, v146
	v_rcp_f32_e32 v147, v147
	v_mul_f32_e32 v132, v132, v182
	v_mul_f32_e32 v133, v133, v183
	v_mul_f32_e32 v134, v134, v184
	v_mul_f32_e32 v135, v135, v185
	v_mul_f32_e32 v136, v136, v186
	v_mul_f32_e32 v137, v137, v187
	v_mul_f32_e32 v138, v138, v188
	v_mul_f32_e32 v139, v139, v189
	v_lshl_add_u64 v[194:195], v[194:195], 0, s[72:73]
	v_mul_f32_e32 v132, v132, v140
	v_mul_f32_e32 v133, v133, v141
	v_mul_f32_e32 v134, v134, v142
	v_mul_f32_e32 v135, v135, v143
	v_mul_f32_e32 v136, v136, v144
	v_mul_f32_e32 v137, v137, v145
	v_mul_f32_e32 v138, v138, v146
	v_mul_f32_e32 v139, v139, v147
	v_cvt_pk_bf16_f32 v190, v132, v133
	v_cvt_pk_bf16_f32 v191, v134, v135
	v_cvt_pk_bf16_f32 v192, v136, v137
	v_cvt_pk_bf16_f32 v193, v138, v139
	global_store_dwordx4 v[194:195], v[190:193], off
	v_min_f32_e32 v132, 0x40e00000, v48
	v_min_f32_e32 v133, 0x40e00000, v49
	v_min_f32_e32 v134, 0x40e00000, v50
	v_min_f32_e32 v135, 0x40e00000, v51
	v_min_f32_e32 v136, 0x40e00000, v44
	v_min_f32_e32 v137, 0x40e00000, v45
	v_min_f32_e32 v138, 0x40e00000, v46
	v_min_f32_e32 v139, 0x40e00000, v47
	v_mul_f32_e32 v140, 0xc01d265f, v132
	v_mul_f32_e32 v141, 0xc01d265f, v133
	v_mul_f32_e32 v142, 0xc01d265f, v134
	v_mul_f32_e32 v143, 0xc01d265f, v135
	v_mul_f32_e32 v144, 0xc01d265f, v136
	v_mul_f32_e32 v145, 0xc01d265f, v137
	v_mul_f32_e32 v146, 0xc01d265f, v138
	v_mul_f32_e32 v147, 0xc01d265f, v139
	v_exp_f32_e32 v140, v140
	v_exp_f32_e32 v141, v141
	v_exp_f32_e32 v142, v142
	v_exp_f32_e32 v143, v143
	v_exp_f32_e32 v144, v144
	v_exp_f32_e32 v145, v145
	v_exp_f32_e32 v146, v146
	v_exp_f32_e32 v147, v147
	v_med3_f32 v182, v16, s4, v198
	v_med3_f32 v183, v17, s4, v198
	v_med3_f32 v184, v18, s4, v198
	v_med3_f32 v185, v19, s4, v198
	v_med3_f32 v186, v12, s4, v198
; __device__ __forceinline__ unsigned cvt_pk_bf16(float lo, float hi) { unsigned r; asm volatile("v_cvt_pk_bf16_f32 %0, %1, %2" : "=v"(r) : "v"(lo), "v"(hi)); return r; }
;     __device__ __forceinline__ void operator()(const pg8::f32x4 (&acc)[2][2][4][2], const pg8::Unit& u, int wr, int wc, int fr, int fq) const {
;     ...
;             for (int m = 0; m < 4; ++m) {
;                 const int row = u.pm + ai * 128 + wr * 64 + m * 16 + fr;
;                 float a[8];
; #pragma unroll
;                 for (int n = 0; n < 2; ++n)
; #pragma unroll
;                     for (int j = 0; j < 4; ++j) {
;                         const float g = fminf(acc[ai][0][m][n][j] + bgv[n][j], 7.f);
;                         const float l = fminf(fmaxf(acc[ai][1][m][n][j] + blv[n][j], -7.f), 7.f);
;                         const float sg = __builtin_amdgcn_rcpf(1.f + __builtin_amdgcn_exp2f(-1.702f * 1.4426950408889634f * g));
;                         a[n * 4 + j] = g * sg * (l + 1.f);
;                     }
;                 pg8::u32x4 w; w.x = pg8::cvt_pk_bf16(a[0], a[1]); w.y = pg8::cvt_pk_bf16(a[2], a[3]); w.z = pg8::cvt_pk_bf16(a[4], a[5]); w.w = pg8::cvt_pk_bf16(a[6], a[7]);
;                 *(pg8::u32x4*)(ACT + (size_t)row * 1024 + colj) = w;
	v_med3_f32 v187, v13, s4, v198
	v_med3_f32 v188, v14, s4, v198
	v_med3_f32 v189, v15, s4, v198
	v_add_f32_e32 v140, 1.0, v140
	v_add_f32_e32 v141, 1.0, v141
	v_add_f32_e32 v142, 1.0, v142
	v_add_f32_e32 v143, 1.0, v143
	v_add_f32_e32 v144, 1.0, v144
	v_add_f32_e32 v145, 1.0, v145
	v_add_f32_e32 v146, 1.0, v146
	v_add_f32_e32 v147, 1.0, v147
	v_rcp_f32_e32 v140, v140
	v_rcp_f32_e32 v141, v141
	v_rcp_f32_e32 v142, v142
	v_rcp_f32_e32 v143, v143
	v_rcp_f32_e32 v144, v144
	v_rcp_f32_e32 v145, v145
	v_rcp_f32_e32 v146, v146
	v_rcp_f32_e32 v147, v147
	v_mul_f32_e32 v132, v132, v182
	v_mul_f32_e32 v133, v133, v183
	v_mul_f32_e32 v134, v134, v184
	v_mul_f32_e32 v135, v135, v185
	v_mul_f32_e32 v136, v136, v186
	v_mul_f32_e32 v137, v137, v187
	v_mul_f32_e32 v138, v138, v188
	v_mul_f32_e32 v139, v139, v189
	v_lshl_add_u64 v[194:195], v[194:195], 0, s[72:73]
	v_mul_f32_e32 v132, v132, v140
	v_mul_f32_e32 v133, v133, v141
	v_mul_f32_e32 v134, v134, v142
	v_mul_f32_e32 v135, v135, v143
	v_mul_f32_e32 v136, v136, v144
	v_mul_f32_e32 v137, v137, v145
	v_mul_f32_e32 v138, v138, v146
	v_mul_f32_e32 v139, v139, v147
	v_cvt_pk_bf16_f32 v190, v132, v133
	v_cvt_pk_bf16_f32 v191, v134, v135
	v_cvt_pk_bf16_f32 v192, v136, v137
	v_cvt_pk_bf16_f32 v193, v138, v139
	global_store_dwordx4 v[194:195], v[190:193], off
	v_min_f32_e32 v132, 0x40e00000, v40
	v_min_f32_e32 v133, 0x40e00000, v41
	v_min_f32_e32 v134, 0x40e00000, v42
	v_min_f32_e32 v135, 0x40e00000, v43
	v_min_f32_e32 v136, 0x40e00000, v36
	v_min_f32_e32 v137, 0x40e00000, v37
	v_min_f32_e32 v138, 0x40e00000, v38
	v_min_f32_e32 v139, 0x40e00000, v39
	v_mul_f32_e32 v140, 0xc01d265f, v132
	v_mul_f32_e32 v141, 0xc01d265f, v133
	v_mul_f32_e32 v142, 0xc01d265f, v134
	v_mul_f32_e32 v143, 0xc01d265f, v135
	v_mul_f32_e32 v144, 0xc01d265f, v136
	v_mul_f32_e32 v145, 0xc01d265f, v137
	v_mul_f32_e32 v146, 0xc01d265f, v138
	v_mul_f32_e32 v147, 0xc01d265f, v139
	v_exp_f32_e32 v140, v140
	v_exp_f32_e32 v141, v141
	v_exp_f32_e32 v142, v142
	v_exp_f32_e32 v143, v143
	v_exp_f32_e32 v144, v144
	v_exp_f32_e32 v145, v145
	v_exp_f32_e32 v146, v146
	v_exp_f32_e32 v147, v147
	v_med3_f32 v182, v8, s4, v198
	v_med3_f32 v183, v9, s4, v198
	v_med3_f32 v184, v10, s4, v198
	v_med3_f32 v185, v11, s4, v198
	v_med3_f32 v186, v4, s4, v198
	v_med3_f32 v187, v5, s4, v198
	v_med3_f32 v188, v6, s4, v198
	v_med3_f32 v189, v7, s4, v198
	v_add_f32_e32 v140, 1.0, v140
	v_add_f32_e32 v141, 1.0, v141
	v_add_f32_e32 v142, 1.0, v142
	v_add_f32_e32 v143, 1.0, v143
	v_add_f32_e32 v144, 1.0, v144
	v_add_f32_e32 v145, 1.0, v145
	v_add_f32_e32 v146, 1.0, v146
	v_add_f32_e32 v147, 1.0, v147
	v_rcp_f32_e32 v140, v140
	v_rcp_f32_e32 v141, v141
	v_rcp_f32_e32 v142, v142
	v_rcp_f32_e32 v143, v143
	v_rcp_f32_e32 v144, v144
	v_rcp_f32_e32 v145, v145
	v_rcp_f32_e32 v146, v146
	v_rcp_f32_e32 v147, v147
	v_mul_f32_e32 v132, v132, v182
	v_mul_f32_e32 v133, v133, v183
	v_mul_f32_e32 v134, v134, v184
	v_mul_f32_e32 v135, v135, v185
	v_mul_f32_e32 v136, v136, v186
	v_mul_f32_e32 v137, v137, v187
	v_mul_f32_e32 v138, v138, v188
	v_mul_f32_e32 v139, v139, v189
	v_lshl_add_u64 v[194:195], v[194:195], 0, s[72:73]
	v_mul_f32_e32 v132, v132, v140
	v_mul_f32_e32 v133, v133, v141
	v_mul_f32_e32 v134, v134, v142
	v_mul_f32_e32 v135, v135, v143
	v_mul_f32_e32 v136, v136, v144
	v_mul_f32_e32 v137, v137, v145
	v_mul_f32_e32 v138, v138, v146
	v_mul_f32_e32 v139, v139, v147
	v_cvt_pk_bf16_f32 v190, v132, v133
	v_cvt_pk_bf16_f32 v191, v134, v135
	v_cvt_pk_bf16_f32 v192, v136, v137
	v_cvt_pk_bf16_f32 v193, v138, v139
	global_store_dwordx4 v[194:195], v[190:193], off
	s_cbranch_vccnz .LBB0_1722
	v_readlane_b32 s82, v255, 1
	v_readlane_b32 s83, v255, 2
	s_branch .LBB0_1697

; __device__ __forceinline__ unsigned cvt_pk_bf16(float lo, float hi) { unsigned r; asm volatile("v_cvt_pk_bf16_f32 %0, %1, %2" : "=v"(r) : "v"(lo), "v"(hi)); return r; }
;     __device__ __forceinline__ void operator()(const pg8::f32x4 (&acc)[2][2][4][2], const pg8::Unit& u, int wr, int wc, int fr, int fq) const {
;     ...
; #pragma unroll
;         for (int ai = 0; ai < 2; ++ai)
; #pragma unroll
;             for (int m = 0; m < 4; ++m) {
;                 bf16_t* rowp = YS + (size_t)(u.pm + ai * 128 + wr * 64 + m * 16 + fr) * 1024 + col0;
; #pragma unroll
;                 for (int bj = 0; bj < 2; ++bj) {
;                     const f32x4 v0 = acc[ai][bj][m][0] + bv[bj][0], v1 = acc[ai][bj][m][1] + bv[bj][1];
;                     pg8::u32x4 w; w.x = pg8::cvt_pk_bf16(v0[0], v0[1]); w.y = pg8::cvt_pk_bf16(v0[2], v0[3]); w.z = pg8::cvt_pk_bf16(v1[0], v1[1]); w.w = pg8::cvt_pk_bf16(v1[2], v1[3]);
;                     *(pg8::u32x4*)(rowp + bj * 128) = w;
;                 }
;             }
.Ldn_epi_nonext:
	s_mov_b64 s[72:73], 0x8000
	s_mov_b64 s[74:75], 0x28000
	s_mov_b64 s[4:5], -1
	s_andn2_b64 vcc, exec, s[42:43]
	v_add_u32_e32 v106, s6, v1
	v_ashrrev_i32_e32 v107, 31, v106
	v_lshlrev_b64 v[104:105], 11, v[106:107]
	v_lshl_add_u64 v[104:105], s[10:11], 0, v[104:105]
	v_lshl_add_u64 v[104:105], v[104:105], 0, v[158:159]
	v_cvt_pk_bf16_f32 v100, v144, v145
	v_cvt_pk_bf16_f32 v101, v146, v147
	v_cvt_pk_bf16_f32 v102, v140, v141
	v_cvt_pk_bf16_f32 v103, v142, v143
	global_store_dwordx4 v[104:105], v[100:103], off
	v_cvt_pk_bf16_f32 v108, v136, v137
	v_cvt_pk_bf16_f32 v109, v138, v139
	v_cvt_pk_bf16_f32 v110, v132, v133
	v_cvt_pk_bf16_f32 v111, v134, v135
	global_store_dwordx4 v[104:105], v[108:111], off offset:256
	v_lshl_add_u64 v[104:105], v[104:105], 0, s[72:73]
	v_cvt_pk_bf16_f32 v100, v128, v129
	v_cvt_pk_bf16_f32 v101, v130, v131
	v_cvt_pk_bf16_f32 v102, v124, v125
	v_cvt_pk_bf16_f32 v103, v126, v127
	global_store_dwordx4 v[104:105], v[100:103], off
	v_cvt_pk_bf16_f32 v108, v120, v121
	v_cvt_pk_bf16_f32 v109, v122, v123
	v_cvt_pk_bf16_f32 v110, v116, v117
	v_cvt_pk_bf16_f32 v111, v118, v119
	global_store_dwordx4 v[104:105], v[108:111], off offset:256
	v_lshl_add_u64 v[104:105], v[104:105], 0, s[72:73]
	v_cvt_pk_bf16_f32 v100, v96, v97
	v_cvt_pk_bf16_f32 v101, v98, v99
	v_cvt_pk_bf16_f32 v102, v92, v93
	v_cvt_pk_bf16_f32 v103, v94, v95
	global_store_dwordx4 v[104:105], v[100:103], off
	v_cvt_pk_bf16_f32 v108, v88, v89
	v_cvt_pk_bf16_f32 v109, v90, v91
	v_cvt_pk_bf16_f32 v110, v84, v85
	v_cvt_pk_bf16_f32 v111, v86, v87
	global_store_dwordx4 v[104:105], v[108:111], off offset:256
	v_lshl_add_u64 v[104:105], v[104:105], 0, s[72:73]
	v_cvt_pk_bf16_f32 v100, v80, v81
	v_cvt_pk_bf16_f32 v101, v82, v83
	v_cvt_pk_bf16_f32 v102, v76, v77
	v_cvt_pk_bf16_f32 v103, v78, v79
	global_store_dwordx4 v[104:105], v[100:103], off
	v_cvt_pk_bf16_f32 v108, v72, v73
	v_cvt_pk_bf16_f32 v109, v74, v75
	v_cvt_pk_bf16_f32 v110, v68, v69
	v_cvt_pk_bf16_f32 v111, v70, v71
	global_store_dwordx4 v[104:105], v[108:111], off offset:256
	v_lshl_add_u64 v[104:105], v[104:105], 0, s[74:75]
	v_cvt_pk_bf16_f32 v100, v64, v65
	v_cvt_pk_bf16_f32 v101, v66, v67
	v_cvt_pk_bf16_f32 v102, v60, v61
	v_cvt_pk_bf16_f32 v103, v62, v63
	global_store_dwordx4 v[104:105], v[100:103], off
	v_cvt_pk_bf16_f32 v108, v56, v57
	v_cvt_pk_bf16_f32 v109, v58, v59
	v_cvt_pk_bf16_f32 v110, v48, v49
	v_cvt_pk_bf16_f32 v111, v50, v51
	global_store_dwordx4 v[104:105], v[108:111], off offset:256
	v_lshl_add_u64 v[104:105], v[104:105], 0, s[72:73]
	v_cvt_pk_bf16_f32 v100, v52, v53
	v_cvt_pk_bf16_f32 v101, v54, v55
	v_cvt_pk_bf16_f32 v102, v44, v45
	v_cvt_pk_bf16_f32 v103, v46, v47
	global_store_dwordx4 v[104:105], v[100:103], off
	v_cvt_pk_bf16_f32 v108, v40, v41
	v_cvt_pk_bf16_f32 v109, v42, v43
	v_cvt_pk_bf16_f32 v110, v32, v33
	v_cvt_pk_bf16_f32 v111, v34, v35
	global_store_dwordx4 v[104:105], v[108:111], off offset:256
	v_lshl_add_u64 v[104:105], v[104:105], 0, s[72:73]
	v_cvt_pk_bf16_f32 v100, v36, v37
	v_cvt_pk_bf16_f32 v101, v38, v39
	v_cvt_pk_bf16_f32 v102, v28, v29
	v_cvt_pk_bf16_f32 v103, v30, v31
	global_store_dwordx4 v[104:105], v[100:103], off
	v_cvt_pk_bf16_f32 v108, v24, v25
	v_cvt_pk_bf16_f32 v109, v26, v27
	v_cvt_pk_bf16_f32 v110, v16, v17
	v_cvt_pk_bf16_f32 v111, v18, v19
	global_store_dwordx4 v[104:105], v[108:111], off offset:256
	v_lshl_add_u64 v[104:105], v[104:105], 0, s[72:73]
	v_cvt_pk_bf16_f32 v100, v20, v21
	v_cvt_pk_bf16_f32 v101, v22, v23
	v_cvt_pk_bf16_f32 v102, v12, v13
	v_cvt_pk_bf16_f32 v103, v14, v15
	global_store_dwordx4 v[104:105], v[100:103], off
	v_cvt_pk_bf16_f32 v108, v8, v9
	v_cvt_pk_bf16_f32 v109, v10, v11
	v_cvt_pk_bf16_f32 v110, v4, v5
	v_cvt_pk_bf16_f32 v111, v6, v7
	global_store_dwordx4 v[104:105], v[108:111], off offset:256
	s_cbranch_vccnz .LBB0_1812
	s_branch .LBB0_1811
